# v34 + waves 0-3 issue the V piece behind the PV section (before the barrier) instead of right after the barrier
# speedup vs baseline: 1.0046x; 1.0017x over previous
; template <bool FOX>
; __device__ __forceinline__ void attn_unit(const Args& A, int b, int h, int qb, LAS char* shm, LAS float* dg) {
;     ...
;         if (t == 1 && 4 < nti) ISSUE_K(t0 + 4, 0);
;         if (t + 4 < nti) ISSUE_K(t0 + t + 4, t % NS);
;         if (t + 2 < nti) ISSUE_V(t0 + t + 2, (t + 2) % NS);
;         SFENCE();
;         { if constexpr (!FOX) { if (t0 + t == tw_last + 1) {
; #pragma unroll
;                   for (int r = 0; r < 16; ++r) negm[r] = -INFINITY;
;                   asm volatile("" : "+v"(negm)); } }
;           const lds_cptr vp = vp0 + ((t - 1) % NS) * VSLOT; float sa = 0.f, sb = 0.f;
; #pragma unroll
;           for (int g = 0; g < 2 * NQ; ++g) {
;               if (!FOX && g == 0) c0 = __builtin_amdgcn_mfma_f32_32x32x16_bf16(kf[0], qr[0], negm, 0, 0, 0);
;               else if (!FOX && g == 1) c1 = __builtin_amdgcn_mfma_f32_32x32x16_bf16(kf[1], qr[0], negm, 0, 0, 0);
;               else if (g & 1) c1 = __builtin_amdgcn_mfma_f32_32x32x16_bf16(kf[g], qr[g >> 1], c1, 0, 0, 0); else c0 = __builtin_amdgcn_mfma_f32_32x32x16_bf16(kf[g], qr[g >> 1], c0, 0, 0, 0);
;               if (g < 8) { const int i = (g >> 1) + 4 * (g & 1); vlo[i] = vtr(vp + (i >> 2) * 4096 + (i & 3) * 1024); vhi[i] = vtr(vp + (i >> 2) * 4096 + (i & 3) * 1024 + 512);
;                   if (g < 4) { sa += pp0[4 * g]; sb += pp0[4 * g + 1]; sa += pp0[4 * g + 2]; sb += pp0[4 * g + 3]; } else { sa += pp1[4 * g - 16]; sb += pp1[4 * g - 15]; sa += pp1[4 * g - 14]; sb += pp1[4 * g - 13]; }
;                   asm volatile("" : "+v"(sa), "+v"(sb)); }
;               { constexpr int G0 = FOX ? 0 : 4; if (g >= G0) { const int q = 2 * (g - G0);
; #pragma unroll
;                   for (int k = 0; k < 2; ++k) { const int w = q + k; const unsigned pkd = w < 8 ? cvt_pk_bf16(pp0[2 * w], pp0[2 * w + 1]) : cvt_pk_bf16(pp1[2 * w - 16], pp1[2 * w - 15]); pw[w >> 2][w & 3] = pkd; } } }
;               SFENCE();
;           }
;           lrun += sa + sb; }
;         MASKONLY(t);
;         float rm; ROWMAX(rm);
;         bool resc = false;
;         if (__any(rm > THR)) { const float dl = fmaxf(rm, 0.f); mhat += dl;
; #pragma unroll
;             for (int r = 0; r < 16; ++r) { c0[r] -= dl; c1[r] -= dl; }
;             if constexpr (!FOX) {
; #pragma unroll
;                 for (int r = 0; r < 16; ++r) negm[r] = -mhat;
;                 asm volatile("" : "+v"(negm)); }
.Lmla_ss1_in:
	s_mov_b32 m0, s52
	s_nop 0
	global_load_lds_dwordx4 v240, s[46:47]
	s_add_i32 m0, s52, 0x2000
	s_nop 0
	global_load_lds_dwordx4 v240, s[98:99]
	s_waitcnt lgkmcnt(0)
	s_add_i32 s27, s42, 0x8000
	v_mfma_f32_32x32x16_bf16 v[114:129], v[206:209], v[138:141], v[82:97]
	s_and_b32 s27, s27, 0x6000
	s_add_u32 s42, s42, 0x2000
	s_addc_u32 s43, s43, 0
	v_add_u32_e32 v3, s27, v247
	ds_read_b64_tr_b16 v[206:207], v3 offset:49152
	ds_read_b64_tr_b16 v[208:209], v3 offset:49664
	v_add_f32_e32 v4, 0, v67
	v_add_f32_e32 v5, 0, v66
	v_add_f32_e32 v4, v69, v4
	v_add_f32_e32 v5, v68, v5
	v_mfma_f32_32x32x16_bf16 v[98:113], v[194:197], v[138:141], v[82:97]
	ds_read_b64_tr_b16 v[194:195], v3 offset:53248
	ds_read_b64_tr_b16 v[196:197], v3 offset:53760
	v_add_f32_e32 v4, v71, v4
	v_add_f32_e32 v5, v70, v5
	v_add_f32_e32 v4, v73, v4
	v_add_f32_e32 v5, v72, v5
	v_mfma_f32_32x32x16_bf16 v[114:129], v[202:205], v[142:145], v[114:129]
	ds_read_b64_tr_b16 v[202:203], v3 offset:50176
	ds_read_b64_tr_b16 v[204:205], v3 offset:50688
	v_add_f32_e32 v4, v75, v4
	v_add_f32_e32 v5, v74, v5
	v_add_f32_e32 v4, v77, v4
	v_add_f32_e32 v5, v76, v5
	v_mfma_f32_32x32x16_bf16 v[98:113], v[186:189], v[142:145], v[98:113]
	ds_read_b64_tr_b16 v[214:215], v3 offset:54272
	ds_read_b64_tr_b16 v[216:217], v3 offset:54784
	v_add_f32_e32 v4, v79, v4
	v_add_f32_e32 v5, v78, v5
	v_add_f32_e32 v4, v81, v4
	v_add_f32_e32 v5, v80, v5
	v_mfma_f32_32x32x16_bf16 v[114:129], v[198:201], v[146:149], v[114:129]
	ds_read_b64_tr_b16 v[210:211], v3 offset:51200
	ds_read_b64_tr_b16 v[212:213], v3 offset:51712
	v_add_f32_e32 v4, v51, v4
	v_add_f32_e32 v5, v50, v5
	v_add_f32_e32 v4, v53, v4
	v_add_f32_e32 v5, v52, v5
	v_mfma_f32_32x32x16_bf16 v[98:113], v[182:185], v[146:149], v[98:113]
	ds_read_b64_tr_b16 v[12:13], v3 offset:55296
	ds_read_b64_tr_b16 v[14:15], v3 offset:55808
	v_add_f32_e32 v4, v55, v4
	v_add_f32_e32 v5, v54, v5
	v_add_f32_e32 v4, v57, v4
	v_add_f32_e32 v5, v56, v5
	v_mfma_f32_32x32x16_bf16 v[114:129], v[190:193], v[150:153], v[114:129]
	ds_read_b64_tr_b16 v[8:9], v3 offset:52224
	ds_read_b64_tr_b16 v[10:11], v3 offset:52736
	v_add_f32_e32 v4, v59, v4
	v_add_f32_e32 v16, v61, v4
	v_add_f32_e32 v4, v58, v5
	v_add_f32_e32 v17, v60, v4
	v_mfma_f32_32x32x16_bf16 v[98:113], v[170:173], v[150:153], v[98:113]
	s_add_u32 s46, s46, s62
	s_addc_u32 s47, s47, s63
	s_and_b32 s64, s26, 3
	ds_read_b64_tr_b16 v[4:5], v3 offset:56320
	ds_read_b64_tr_b16 v[6:7], v3 offset:56832
	v_add_f32_e32 v3, v63, v16
	v_add_f32_e32 v16, v62, v17
	v_add_f32_e32 v3, v65, v3
	v_add_f32_e32 v16, v64, v16
	v_mfma_f32_32x32x16_bf16 v[114:129], v[178:181], v[154:157], v[114:129]
	s_mulk_i32 s64, 0x3000
	v_cvt_pk_bf16_f32 v178, v50, v51
	v_cvt_pk_bf16_f32 v179, v52, v53
	v_cvt_pk_bf16_f32 v186, v66, v67
	v_cvt_pk_bf16_f32 v187, v68, v69
	v_mfma_f32_32x32x16_bf16 v[98:113], v[166:169], v[154:157], v[98:113]
	s_add_i32 s52, s64, s91
	s_add_i32 s64, s42, 0x6000
	s_add_u32 s98, s98, s62
	s_addc_u32 s99, s99, s63
	v_cvt_pk_bf16_f32 v180, v54, v55
	v_cvt_pk_bf16_f32 v181, v56, v57
	v_cvt_pk_bf16_f32 v188, v70, v71
	v_cvt_pk_bf16_f32 v189, v72, v73
	v_mfma_f32_32x32x16_bf16 v[114:129], v[174:177], v[158:161], v[114:129]
	s_and_b32 s64, s64, 0x6000
	s_add_i32 s65, s64, s93
	v_cvt_pk_bf16_f32 v218, v58, v59
	v_cvt_pk_bf16_f32 v219, v60, v61
	v_cvt_pk_bf16_f32 v182, v74, v75
	v_cvt_pk_bf16_f32 v183, v76, v77
	v_mfma_f32_32x32x16_bf16 v[98:113], v[162:165], v[158:161], v[98:113]
	v_cvt_pk_bf16_f32 v220, v62, v63
	v_cvt_pk_bf16_f32 v221, v64, v65
	v_cvt_pk_bf16_f32 v184, v78, v79
	v_cvt_pk_bf16_f32 v185, v80, v81
	v_add_f32_e32 v3, v3, v16
	v_add_f32_e32 v246, v246, v3
	s_nop 3
	s_waitcnt lgkmcnt(0)
	v_mfma_f32_32x32x16_bf16 v[18:33], v[186:189], v[206:209], v[18:33]
	s_add_i32 s27, s26, 1
	s_and_b32 s64, s27, 3
	s_mulk_i32 s64, 0x3000
	v_exp_f32_e32 v66, v114
	v_exp_f32_e32 v67, v115
	v_exp_f32_e32 v68, v116
	v_exp_f32_e32 v69, v117
	v_add_u32_e32 v3, s64, v248
	v_mfma_f32_32x32x16_bf16 v[34:49], v[186:189], v[194:197], v[34:49]
	v_exp_f32_e32 v70, v118
	v_exp_f32_e32 v71, v119
	v_exp_f32_e32 v72, v120
	v_exp_f32_e32 v73, v121
	ds_read_b128 v[206:209], v3
	ds_read_b128 v[194:197], v3 offset:512
	v_mfma_f32_32x32x16_bf16 v[18:33], v[182:185], v[202:205], v[18:33]
	v_exp_f32_e32 v74, v122
	v_exp_f32_e32 v75, v123
	v_exp_f32_e32 v76, v124
	v_exp_f32_e32 v77, v125
	ds_read_b128 v[202:205], v3 offset:2048
	ds_read_b128 v[186:189], v3 offset:2560
	v_mfma_f32_32x32x16_bf16 v[34:49], v[182:185], v[214:217], v[34:49]
	v_exp_f32_e32 v78, v126
	v_exp_f32_e32 v79, v127
	v_exp_f32_e32 v80, v128
	v_exp_f32_e32 v81, v129
	ds_read_b128 v[198:201], v3 offset:4096
	ds_read_b128 v[182:185], v3 offset:4608
	v_mfma_f32_32x32x16_bf16 v[18:33], v[178:181], v[210:213], v[18:33]
	v_exp_f32_e32 v50, v98
	v_exp_f32_e32 v51, v99
	v_exp_f32_e32 v52, v100
	v_exp_f32_e32 v53, v101
	ds_read_b128 v[190:193], v3 offset:6144
	ds_read_b128 v[170:173], v3 offset:6656
	v_mfma_f32_32x32x16_bf16 v[34:49], v[178:181], v[12:15], v[34:49]
	v_exp_f32_e32 v54, v102
	v_exp_f32_e32 v55, v103
	v_exp_f32_e32 v56, v104
	v_exp_f32_e32 v57, v105
	ds_read_b128 v[178:181], v3 offset:8192
	ds_read_b128 v[166:169], v3 offset:8704
	v_mfma_f32_32x32x16_bf16 v[18:33], v[218:221], v[8:11], v[18:33]
	v_exp_f32_e32 v58, v106
	v_exp_f32_e32 v59, v107
	v_exp_f32_e32 v60, v108
	v_exp_f32_e32 v61, v109
	ds_read_b128 v[174:177], v3 offset:10240
	ds_read_b128 v[162:165], v3 offset:10752
	v_mfma_f32_32x32x16_bf16 v[34:49], v[218:221], v[4:7], v[34:49]
	v_exp_f32_e32 v62, v110
	v_exp_f32_e32 v63, v111
	v_exp_f32_e32 v64, v112
	v_exp_f32_e32 v65, v113
	s_mov_b32 m0, s53
	s_mov_b32 s53, s65
	global_load_lds_dwordx4 v240, s[60:61]
	s_add_u32 s60, s60, 0x2000
	s_addc_u32 s61, s61, 0
	s_mov_b32 s26, s27
	s_cmp_eq_u32 s27, s96
	s_cbranch_scc1 .Lmla_ss1_xdone
	s_add_i32 s64, s27, 3
	s_cmp_lt_u32 s64, s94
	s_cbranch_scc1 .Lmla_ss1_top
	s_waitcnt vmcnt(4)
	s_barrier
	s_branch .Lmla_ss_back
